# baseline (speedup 1.0000x reference)
_Z16node_post_kernelPKfS0_PKtS0_S2_S0_S0_S0_S0_S0_Pf:
	s_load_dwordx16 s[4:19], s[0:1], 0x0
	s_load_dwordx4 s[20:23], s[0:1], 0x40
	s_load_dwordx2 s[24:25], s[0:1], 0x50
	v_lshrrev_b32_e32 v5, 6, v0
	v_and_b32_e32 v1, 63, v0
	v_and_b32_e32 v2, 15, v0
	v_bfe_u32 v3, v0, 4, 2
	v_readfirstlane_b32 s26, v5
	v_lshlrev_b32_e32 v4, 4, v1
	v_lshlrev_b32_e32 v6, 5, v1
	v_add_u32_e32 v7, 0x1000, v6
	v_lshlrev_b32_e32 v8, 2, v1
	v_add_u32_e32 v9, 0x1000, v4
	v_add_u32_e32 v10, 0x2000, v4
	v_add_u32_e32 v11, 0x3000, v4
	v_lshlrev_b32_e32 v12, 7, v5
	v_lshl_or_b32 v12, v3, 4, v12
	v_and_b32_e32 v13, 1, v2
	v_lshl_or_b32 v13, v13, 10, v12
	v_mov_b32_e32 v14, 0xff7fffff
	v_cmp_gt_u32_e64 s[58:59], 2, v2
	s_lshl_b32 s27, s2, 1
	s_lshr_b32 s28, s2, 7
	s_and_b32 s29, s26, 1
	s_add_u32 s32, s27, s29
	s_lshl_b32 s32, s32, 13
	s_lshr_b32 s33, s26, 1
	s_lshl_b32 s33, s33, 3
	s_add_u32 s32, s32, s33
	s_lshl_b32 s60, s26, 14
	s_lshl_b32 s61, s28, 17
	s_add_u32 s61, s61, s60
	s_lshl_b32 s62, s28, 10
	s_lshl_b32 s63, s27, 10
	s_waitcnt lgkmcnt(0)
	s_add_u32 s30, s4, s32
	s_addc_u32 s31, s5, 0
	s_add_u32 s34, s6, s62
	s_addc_u32 s35, s7, 0
	s_add_u32 s36, s8, s61
	s_addc_u32 s37, s9, 0
	s_add_u32 s38, s12, s60
	s_addc_u32 s39, s13, 0
	s_add_u32 s40, s38, 0x20000
	s_addc_u32 s41, s39, 0
	s_add_u32 s42, s38, 0x40000
	s_addc_u32 s43, s39, 0
	s_add_u32 s44, s10, s63
	s_addc_u32 s45, s11, 0
	s_add_u32 s46, s24, s63
	s_addc_u32 s47, s25, 0
	global_load_dwordx2 v[56:57], v6, s[30:31]
	global_load_dwordx2 v[58:59], v6, s[30:31] offset:2048
	global_load_dwordx2 v[60:61], v7, s[30:31]
	global_load_dwordx2 v[62:63], v7, s[30:31] offset:2048
	global_load_dword v40, v8, s[34:35]
	global_load_dword v41, v8, s[34:35] offset:256
	global_load_dword v42, v8, s[34:35] offset:512
	global_load_dword v43, v8, s[34:35] offset:768
	s_lshr_b32 s64, s2, 3
	s_and_b32 s64, s64, 31
	s_and_b32 s65, s64, 15
	s_lshl_b32 s65, s65, 13
	s_lshl_b32 s66, s28, 17
	s_add_u32 s65, s65, s66
	s_lshl_b32 s67, s26, 10
	s_add_u32 s65, s65, s67
	s_add_u32 s68, s8, s65
	s_addc_u32 s69, s9, 0
	s_mul_i32 s66, s64, 0x3000
	s_lshl_b32 s67, s26, 11
	s_min_u32 s67, s67, 0x2800
	s_add_u32 s66, s66, s67
	s_add_u32 s70, s12, s66
	s_addc_u32 s71, s13, 0
	global_load_dwordx4 v[192:195], v4, s[68:69]
	global_load_dwordx4 v[196:199], v4, s[70:71]
	global_load_dwordx4 v[200:203], v4, s[70:71] offset:1024
	global_load_dwordx4 v[16:19], v12, s[14:15]
	global_load_dwordx4 v[20:23], v12, s[14:15] offset:64
	global_load_dwordx4 v[24:27], v13, s[44:45]
	global_load_dwordx4 v[28:31], v13, s[44:45] offset:64
	global_load_dwordx4 v[32:35], v4, s[16:17]
	global_load_dwordx4 v[36:39], v4, s[18:19]
	v_lshlrev_b32_e32 v15, 1, v1
	s_lshl_b32 s48, s29, 12
	s_lshl_b32 s49, s33, 7
	s_add_u32 s48, s48, s49
	v_add_u32_e32 v15, s48, v15
	s_waitcnt vmcnt(9)
	v_cmp_neq_f32_e64 s[50:51], 0, v40
	v_cmp_neq_f32_e64 s[52:53], 0, v41
	v_cmp_neq_f32_e64 s[54:55], 0, v42
	v_cmp_neq_f32_e64 s[56:57], 0, v43
	v_cndmask_b32_e64 v56, v14, v56, s[50:51]
	v_cndmask_b32_e64 v57, v14, v57, s[50:51]
	v_cndmask_b32_e64 v58, v14, v58, s[52:53]
	v_cndmask_b32_e64 v59, v14, v59, s[52:53]
	v_cndmask_b32_e64 v60, v14, v60, s[54:55]
	v_cndmask_b32_e64 v61, v14, v61, s[54:55]
	v_cndmask_b32_e64 v62, v14, v62, s[56:57]
	v_cndmask_b32_e64 v63, v14, v63, s[56:57]
	v_max_f32_e32 v40, v56, v58
	v_max_f32_e32 v41, v57, v59
	v_max3_f32 v40, v40, v60, v62
	v_max3_f32 v41, v41, v61, v63
	s_nop 1
	v_max_f32_dpp v40, v40, v40 quad_perm:[1,0,3,2] row_mask:0xf bank_mask:0xf
	v_max_f32_dpp v41, v41, v41 quad_perm:[1,0,3,2] row_mask:0xf bank_mask:0xf
	s_nop 1
	v_max_f32_dpp v40, v40, v40 quad_perm:[2,3,0,1] row_mask:0xf bank_mask:0xf
	v_max_f32_dpp v41, v41, v41 quad_perm:[2,3,0,1] row_mask:0xf bank_mask:0xf
	s_nop 1
	v_max_f32_dpp v40, v40, v40 row_half_mirror row_mask:0xf bank_mask:0xf
	v_max_f32_dpp v41, v41, v41 row_half_mirror row_mask:0xf bank_mask:0xf
	s_nop 1
	v_max_f32_dpp v40, v40, v40 row_mirror row_mask:0xf bank_mask:0xf
	v_max_f32_dpp v41, v41, v41 row_mirror row_mask:0xf bank_mask:0xf
	s_nop 1
	v_mov_b32_e32 v42, v40
	v_mov_b32_e32 v43, v41
	s_nop 1
	v_permlane16_swap_b32_e32 v40, v42
	v_permlane16_swap_b32_e32 v41, v43
	v_max_f32_e32 v40, v40, v42
	v_max_f32_e32 v41, v41, v43
	v_mov_b32_e32 v42, v40
	v_mov_b32_e32 v43, v41
	s_nop 1
	v_permlane32_swap_b32_e32 v40, v42
	v_permlane32_swap_b32_e32 v41, v43
	v_max_f32_e32 v40, v40, v42
	v_max_f32_e32 v41, v41, v43
	v_sub_f32_e32 v56, v56, v40
	v_sub_f32_e32 v57, v57, v41
	v_sub_f32_e32 v58, v58, v40
	v_sub_f32_e32 v59, v59, v41
	v_sub_f32_e32 v60, v60, v40
	v_sub_f32_e32 v61, v61, v41
	v_sub_f32_e32 v62, v62, v40
	v_sub_f32_e32 v63, v63, v41
	v_mul_f32_e32 v56, 0x3fb8aa3b, v56
	v_mul_f32_e32 v57, 0x3fb8aa3b, v57
	v_mul_f32_e32 v58, 0x3fb8aa3b, v58
	v_mul_f32_e32 v59, 0x3fb8aa3b, v59
	v_mul_f32_e32 v60, 0x3fb8aa3b, v60
	v_mul_f32_e32 v61, 0x3fb8aa3b, v61
	v_mul_f32_e32 v62, 0x3fb8aa3b, v62
	v_mul_f32_e32 v63, 0x3fb8aa3b, v63
	v_exp_f32_e32 v56, v56
	v_exp_f32_e32 v57, v57
	v_exp_f32_e32 v58, v58
	v_exp_f32_e32 v59, v59
	v_exp_f32_e32 v60, v60
	v_exp_f32_e32 v61, v61
	v_exp_f32_e32 v62, v62
	v_exp_f32_e32 v63, v63
	s_nop 0
	v_add_f32_e32 v44, v56, v58
	v_add_f32_e32 v45, v57, v59
	v_add_f32_e32 v44, v44, v60
	v_add_f32_e32 v45, v45, v61
	v_add_f32_e32 v44, v44, v62
	v_add_f32_e32 v45, v45, v63
	s_nop 1
	v_add_f32_dpp v44, v44, v44 quad_perm:[1,0,3,2] row_mask:0xf bank_mask:0xf
	v_add_f32_dpp v45, v45, v45 quad_perm:[1,0,3,2] row_mask:0xf bank_mask:0xf
	s_nop 1
	v_add_f32_dpp v44, v44, v44 quad_perm:[2,3,0,1] row_mask:0xf bank_mask:0xf
	v_add_f32_dpp v45, v45, v45 quad_perm:[2,3,0,1] row_mask:0xf bank_mask:0xf
	s_nop 1
	v_add_f32_dpp v44, v44, v44 row_half_mirror row_mask:0xf bank_mask:0xf
	v_add_f32_dpp v45, v45, v45 row_half_mirror row_mask:0xf bank_mask:0xf
	s_nop 1
	v_add_f32_dpp v44, v44, v44 row_mirror row_mask:0xf bank_mask:0xf
	v_add_f32_dpp v45, v45, v45 row_mirror row_mask:0xf bank_mask:0xf
	s_nop 1
	v_mov_b32_e32 v42, v44
	v_mov_b32_e32 v43, v45
	s_nop 1
	v_permlane16_swap_b32_e32 v44, v42
	v_permlane16_swap_b32_e32 v45, v43
	v_add_f32_e32 v44, v44, v42
	v_add_f32_e32 v45, v45, v43
	v_mov_b32_e32 v42, v44
	v_mov_b32_e32 v43, v45
	s_nop 1
	v_permlane32_swap_b32_e32 v44, v42
	v_permlane32_swap_b32_e32 v45, v43
	v_add_f32_e32 v44, v44, v42
	v_add_f32_e32 v45, v45, v43
	v_rcp_f32_e32 v46, v44
	v_rcp_f32_e32 v47, v45
	s_nop 0
	v_fma_f32 v42, -v44, v46, 1.0
	v_fma_f32 v43, -v45, v47, 1.0
	v_fma_f32 v46, v42, v46, v46
	v_fma_f32 v47, v43, v47, v47
	v_mul_f32_e32 v56, v56, v46
	v_mul_f32_e32 v57, v57, v47
	v_mul_f32_e32 v58, v58, v46
	v_mul_f32_e32 v59, v59, v47
	v_mul_f32_e32 v60, v60, v46
	v_mul_f32_e32 v61, v61, v47
	v_mul_f32_e32 v62, v62, v46
	v_mul_f32_e32 v63, v63, v47
	v_cvt_pk_bf16_f32 v48, v56, v57
	v_cvt_pk_bf16_f32 v49, v58, v59
	v_cvt_pk_bf16_f32 v50, v60, v61
	v_cvt_pk_bf16_f32 v51, v62, v63
	ds_write_b16 v15, v48 offset:0
	ds_write_b16_d16_hi v15, v48 offset:512
	ds_write_b16 v15, v49 offset:128
	ds_write_b16_d16_hi v15, v49 offset:640
	ds_write_b16 v15, v50 offset:256
	ds_write_b16_d16_hi v15, v50 offset:768
	ds_write_b16 v15, v51 offset:384
	ds_write_b16_d16_hi v15, v51 offset:896
	v_lshlrev_b32_e32 v6, 12, v2
	v_lshl_or_b32 v6, v5, 9, v6
	v_lshl_or_b32 v6, v3, 4, v6
	v_lshlrev_b32_e32 v7, 9, v2
	v_lshl_or_b32 v7, v3, 4, v7
	v_lshlrev_b32_e32 v8, 9, v2
	v_lshl_or_b32 v8, v5, 6, v8
	v_lshl_or_b32 v8, v3, 3, v8
	v_mov_b32_e32 v40, 0
	v_mov_b32_e32 v41, 0
	v_mov_b32_e32 v42, 0
	v_mov_b32_e32 v43, 0
	v_mov_b32_e32 v44, 0
	v_mov_b32_e32 v45, 0
	v_mov_b32_e32 v46, 0
	v_mov_b32_e32 v47, 0
	v_mov_b32_e32 v48, 0
	v_mov_b32_e32 v49, 0
	v_mov_b32_e32 v50, 0
	v_mov_b32_e32 v51, 0
	v_mov_b32_e32 v52, 0
	v_mov_b32_e32 v53, 0
	v_mov_b32_e32 v54, 0
	v_mov_b32_e32 v55, 0
	s_waitcnt lgkmcnt(0)
	s_barrier
	global_load_dwordx4 v[64:67], v4, s[36:37]
	global_load_dwordx4 v[68:71], v4, s[36:37] offset:1024
	global_load_dwordx4 v[72:75], v4, s[36:37] offset:2048
	global_load_dwordx4 v[76:79], v4, s[36:37] offset:3072
	global_load_dwordx4 v[80:83], v9, s[36:37]
	global_load_dwordx4 v[84:87], v9, s[36:37] offset:1024
	global_load_dwordx4 v[88:91], v9, s[36:37] offset:2048
	global_load_dwordx4 v[92:95], v9, s[36:37] offset:3072
	global_load_dwordx4 v[96:99], v10, s[36:37]
	global_load_dwordx4 v[100:103], v10, s[36:37] offset:1024
	global_load_dwordx4 v[104:107], v10, s[36:37] offset:2048
	global_load_dwordx4 v[108:111], v10, s[36:37] offset:3072
	global_load_dwordx4 v[112:115], v11, s[36:37]
	global_load_dwordx4 v[116:119], v11, s[36:37] offset:1024
	global_load_dwordx4 v[120:123], v11, s[36:37] offset:2048
	global_load_dwordx4 v[124:127], v11, s[36:37] offset:3072
	global_load_dwordx4 v[128:131], v4, s[38:39]
	global_load_dwordx4 v[132:135], v4, s[38:39] offset:1024
	global_load_dwordx4 v[136:139], v4, s[38:39] offset:2048
	global_load_dwordx4 v[140:143], v4, s[38:39] offset:3072
	global_load_dwordx4 v[144:147], v9, s[38:39]
	global_load_dwordx4 v[148:151], v9, s[38:39] offset:1024
	global_load_dwordx4 v[152:155], v9, s[38:39] offset:2048
	global_load_dwordx4 v[156:159], v9, s[38:39] offset:3072
	global_load_dwordx4 v[160:163], v10, s[38:39]
	global_load_dwordx4 v[164:167], v10, s[38:39] offset:1024
	global_load_dwordx4 v[168:171], v10, s[38:39] offset:2048
	global_load_dwordx4 v[172:175], v10, s[38:39] offset:3072
	global_load_dwordx4 v[176:179], v11, s[38:39]
	global_load_dwordx4 v[180:183], v11, s[38:39] offset:1024
	global_load_dwordx4 v[184:187], v11, s[38:39] offset:2048
	global_load_dwordx4 v[188:191], v11, s[38:39] offset:3072
	global_load_dwordx4 v[192:195], v4, s[40:41]
	global_load_dwordx4 v[196:199], v4, s[40:41] offset:1024
	global_load_dwordx4 v[200:203], v4, s[40:41] offset:2048
	global_load_dwordx4 v[204:207], v4, s[40:41] offset:3072
	global_load_dwordx4 v[208:211], v9, s[40:41]
	global_load_dwordx4 v[212:215], v9, s[40:41] offset:1024
	global_load_dwordx4 v[216:219], v9, s[40:41] offset:2048
	global_load_dwordx4 v[220:223], v9, s[40:41] offset:3072
	global_load_dwordx4 v[224:227], v10, s[40:41]
	global_load_dwordx4 v[228:231], v10, s[40:41] offset:1024
	global_load_dwordx4 v[232:235], v10, s[40:41] offset:2048
	global_load_dwordx4 v[236:239], v10, s[40:41] offset:3072
	global_load_dwordx4 v[240:243], v11, s[40:41]
	global_load_dwordx4 v[244:247], v11, s[40:41] offset:1024
	global_load_dwordx4 v[248:251], v11, s[40:41] offset:2048
	global_load_dwordx4 v[252:255], v11, s[40:41] offset:3072
	s_waitcnt vmcnt(32)
	s_mov_b64 exec, s[58:59]
	ds_read_b128 v[40:43], v6 offset:0
	ds_read_b128 v[44:47], v6 offset:64
	ds_read_b128 v[48:51], v6 offset:128
	ds_read_b128 v[52:55], v6 offset:192
	s_mov_b64 exec, -1
	s_waitcnt lgkmcnt(0)
	v_mfma_f32_16x16x32_bf16 v[56:59], v[64:67], v[40:43], 0
	v_mfma_f32_16x16x32_bf16 v[60:63], v[96:99], v[40:43], 0
	v_mfma_f32_16x16x32_bf16 v[56:59], v[68:71], v[44:47], v[56:59]
	v_mfma_f32_16x16x32_bf16 v[60:63], v[100:103], v[44:47], v[60:63]
	v_mfma_f32_16x16x32_bf16 v[56:59], v[72:75], v[48:51], v[56:59]
	v_mfma_f32_16x16x32_bf16 v[60:63], v[104:107], v[48:51], v[60:63]
	v_mfma_f32_16x16x32_bf16 v[56:59], v[76:79], v[52:55], v[56:59]
	v_mfma_f32_16x16x32_bf16 v[60:63], v[108:111], v[52:55], v[60:63]
	s_mov_b64 exec, s[58:59]
	ds_read_b128 v[40:43], v6 offset:256
	ds_read_b128 v[44:47], v6 offset:320
	ds_read_b128 v[48:51], v6 offset:384
	ds_read_b128 v[52:55], v6 offset:448
	s_mov_b64 exec, -1
	s_waitcnt lgkmcnt(0)
	v_mfma_f32_16x16x32_bf16 v[56:59], v[80:83], v[40:43], v[56:59]
	v_mfma_f32_16x16x32_bf16 v[60:63], v[112:115], v[40:43], v[60:63]
	v_mfma_f32_16x16x32_bf16 v[56:59], v[84:87], v[44:47], v[56:59]
	v_mfma_f32_16x16x32_bf16 v[60:63], v[116:119], v[44:47], v[60:63]
	v_mfma_f32_16x16x32_bf16 v[56:59], v[88:91], v[48:51], v[56:59]
	v_mfma_f32_16x16x32_bf16 v[60:63], v[120:123], v[48:51], v[60:63]
	v_mfma_f32_16x16x32_bf16 v[56:59], v[92:95], v[52:55], v[56:59]
	v_mfma_f32_16x16x32_bf16 v[60:63], v[124:127], v[52:55], v[60:63]
	s_nop 9
	v_cvt_pk_bf16_f32 v48, v56, v57
	v_cvt_pk_bf16_f32 v49, v58, v59
	v_cvt_pk_bf16_f32 v50, v60, v61
	v_cvt_pk_bf16_f32 v51, v62, v63
	s_mov_b64 exec, s[58:59]
	ds_write_b64 v8, v[48:49] offset:8192
	ds_write_b64 v8, v[50:51] offset:8224
	s_mov_b64 exec, -1
	global_load_dwordx4 v[64:67], v4, s[42:43]
	global_load_dwordx4 v[68:71], v4, s[42:43] offset:1024
	global_load_dwordx4 v[72:75], v4, s[42:43] offset:2048
	global_load_dwordx4 v[76:79], v4, s[42:43] offset:3072
	global_load_dwordx4 v[80:83], v9, s[42:43]
	global_load_dwordx4 v[84:87], v9, s[42:43] offset:1024
	global_load_dwordx4 v[88:91], v9, s[42:43] offset:2048
	global_load_dwordx4 v[92:95], v9, s[42:43] offset:3072
	global_load_dwordx4 v[96:99], v10, s[42:43]
	global_load_dwordx4 v[100:103], v10, s[42:43] offset:1024
	global_load_dwordx4 v[104:107], v10, s[42:43] offset:2048
	global_load_dwordx4 v[108:111], v10, s[42:43] offset:3072
	global_load_dwordx4 v[112:115], v11, s[42:43]
	global_load_dwordx4 v[116:119], v11, s[42:43] offset:1024
	global_load_dwordx4 v[120:123], v11, s[42:43] offset:2048
	global_load_dwordx4 v[124:127], v11, s[42:43] offset:3072
	v_lshlrev_b32_e32 v15, 10, v2
	v_add_u32_e32 v15, v15, v12
	v_mov_b32_e32 v48, 0
	v_mov_b32_e32 v49, 0
	v_mov_b32_e32 v50, 0
	v_mov_b32_e32 v51, 0
	s_waitcnt lgkmcnt(0)
	s_barrier
	s_waitcnt vmcnt(32)
	s_mov_b64 exec, s[58:59]
	ds_read_b128 v[40:43], v7 offset:8192
	ds_read_b128 v[44:47], v7 offset:8256
	ds_read_b128 v[48:51], v7 offset:8320
	ds_read_b128 v[52:55], v7 offset:8384
	s_mov_b64 exec, -1
	s_waitcnt lgkmcnt(0)
	v_mfma_f32_16x16x32_bf16 v[56:59], v[128:131], v[40:43], 0
	v_mfma_f32_16x16x32_bf16 v[60:63], v[160:163], v[40:43], 0
	v_mfma_f32_16x16x32_bf16 v[56:59], v[132:135], v[44:47], v[56:59]
	v_mfma_f32_16x16x32_bf16 v[60:63], v[164:167], v[44:47], v[60:63]
	v_mfma_f32_16x16x32_bf16 v[56:59], v[136:139], v[48:51], v[56:59]
	v_mfma_f32_16x16x32_bf16 v[60:63], v[168:171], v[48:51], v[60:63]
	v_mfma_f32_16x16x32_bf16 v[56:59], v[140:143], v[52:55], v[56:59]
	v_mfma_f32_16x16x32_bf16 v[60:63], v[172:175], v[52:55], v[60:63]
	s_mov_b64 exec, s[58:59]
	ds_read_b128 v[40:43], v7 offset:8448
	ds_read_b128 v[44:47], v7 offset:8512
	ds_read_b128 v[48:51], v7 offset:8576
	ds_read_b128 v[52:55], v7 offset:8640
	s_mov_b64 exec, -1
	s_waitcnt lgkmcnt(0)
	v_mfma_f32_16x16x32_bf16 v[56:59], v[144:147], v[40:43], v[56:59]
	v_mfma_f32_16x16x32_bf16 v[60:63], v[176:179], v[40:43], v[60:63]
	v_mfma_f32_16x16x32_bf16 v[56:59], v[148:151], v[44:47], v[56:59]
	v_mfma_f32_16x16x32_bf16 v[60:63], v[180:183], v[44:47], v[60:63]
	v_mfma_f32_16x16x32_bf16 v[56:59], v[152:155], v[48:51], v[56:59]
	v_mfma_f32_16x16x32_bf16 v[60:63], v[184:187], v[48:51], v[60:63]
	v_mfma_f32_16x16x32_bf16 v[56:59], v[156:159], v[52:55], v[56:59]
	v_mfma_f32_16x16x32_bf16 v[60:63], v[188:191], v[52:55], v[60:63]
	s_nop 9
	v_add_f32_e32 v56, v56, v16
	v_add_f32_e32 v57, v57, v17
	v_add_f32_e32 v58, v58, v18
	v_add_f32_e32 v59, v59, v19
	v_add_f32_e32 v60, v60, v20
	v_add_f32_e32 v61, v61, v21
	v_add_f32_e32 v62, v62, v22
	v_add_f32_e32 v63, v63, v23
	v_add_f32_e32 v24, v56, v24
	v_add_f32_e32 v25, v57, v25
	v_add_f32_e32 v26, v58, v26
	v_add_f32_e32 v27, v59, v27
	v_add_f32_e32 v28, v60, v28
	v_add_f32_e32 v29, v61, v29
	v_add_f32_e32 v30, v62, v30
	v_add_f32_e32 v31, v63, v31
	s_mov_b64 exec, s[58:59]
	ds_write_b128 v15, v[24:27] offset:10240
	ds_write_b128 v15, v[28:31] offset:10304
	s_mov_b64 exec, -1
	global_load_dwordx4 v[16:19], v12, s[20:21]
	global_load_dwordx4 v[20:23], v12, s[20:21] offset:64
	s_waitcnt lgkmcnt(0)
	s_barrier
	s_cmp_gt_u32 s26, 1
	s_cbranch_scc1 .Lnp_ln_done
	s_lshl_b32 s48, s26, 10
	v_add_u32_e32 v40, s48, v4
	ds_read_b128 v[44:47], v40 offset:10240
	s_waitcnt lgkmcnt(0)
	v_add_f32_e32 v41, v44, v45
	v_add_f32_e32 v41, v41, v46
	v_add_f32_e32 v41, v41, v47
	s_nop 1
	v_add_f32_dpp v41, v41, v41 quad_perm:[1,0,3,2] row_mask:0xf bank_mask:0xf
	s_nop 1
	v_add_f32_dpp v41, v41, v41 quad_perm:[2,3,0,1] row_mask:0xf bank_mask:0xf
	s_nop 1
	v_add_f32_dpp v41, v41, v41 row_half_mirror row_mask:0xf bank_mask:0xf
	s_nop 1
	v_add_f32_dpp v41, v41, v41 row_mirror row_mask:0xf bank_mask:0xf
	s_nop 1
	v_mov_b32_e32 v42, v41
	s_nop 1
	v_permlane16_swap_b32_e32 v41, v42
	v_add_f32_e32 v41, v41, v42
	v_mov_b32_e32 v42, v41
	s_nop 1
	v_permlane32_swap_b32_e32 v41, v42
	v_add_f32_e32 v41, v41, v42
	v_mul_f32_e32 v41, 0x3b800000, v41
	v_sub_f32_e32 v44, v44, v41
	v_sub_f32_e32 v45, v45, v41
	v_sub_f32_e32 v46, v46, v41
	v_sub_f32_e32 v47, v47, v41
	v_mul_f32_e32 v43, v44, v44
	v_fmac_f32_e32 v43, v45, v45
	v_fmac_f32_e32 v43, v46, v46
	v_fmac_f32_e32 v43, v47, v47
	s_nop 1
	v_add_f32_dpp v43, v43, v43 quad_perm:[1,0,3,2] row_mask:0xf bank_mask:0xf
	s_nop 1
	v_add_f32_dpp v43, v43, v43 quad_perm:[2,3,0,1] row_mask:0xf bank_mask:0xf
	s_nop 1
	v_add_f32_dpp v43, v43, v43 row_half_mirror row_mask:0xf bank_mask:0xf
	s_nop 1
	v_add_f32_dpp v43, v43, v43 row_mirror row_mask:0xf bank_mask:0xf
	s_nop 1
	v_mov_b32_e32 v42, v43
	s_nop 1
	v_permlane16_swap_b32_e32 v43, v42
	v_add_f32_e32 v43, v43, v42
	v_mov_b32_e32 v42, v43
	s_nop 1
	v_permlane32_swap_b32_e32 v43, v42
	v_add_f32_e32 v43, v43, v42
	v_mov_b32_e32 v42, 0x3727c5ac
	v_fmac_f32_e32 v42, 0x3b800000, v43
	v_rsq_f32_e32 v42, v42
	s_nop 0
	v_mul_f32_e32 v44, v44, v42
	v_mul_f32_e32 v45, v45, v42
	v_mul_f32_e32 v46, v46, v42
	v_mul_f32_e32 v47, v47, v42
	v_fma_f32 v44, v44, v32, v36
	v_fma_f32 v45, v45, v33, v37
	v_fma_f32 v46, v46, v34, v38
	v_fma_f32 v47, v47, v35, v39
	v_cvt_pk_bf16_f32 v48, v44, v45
	v_cvt_pk_bf16_f32 v49, v46, v47
	s_lshl_b32 s48, s26, 9
	v_lshlrev_b32_e32 v40, 3, v1
	v_add_u32_e32 v40, s48, v40
	ds_write_b64 v40, v[48:49] offset:8192
	v_mov_b32_e32 v40, 0
	v_mov_b32_e32 v41, 0
	v_mov_b32_e32 v42, 0
	v_mov_b32_e32 v43, 0
	v_mov_b32_e32 v44, 0
	v_mov_b32_e32 v45, 0
	v_mov_b32_e32 v46, 0
	v_mov_b32_e32 v47, 0
	v_mov_b32_e32 v48, 0
	v_mov_b32_e32 v49, 0
	v_mov_b32_e32 v50, 0
	v_mov_b32_e32 v51, 0
